# hot loop heads (GEMM K-loops, attention, V loops) aligned to 128 bytes
# baseline (speedup 1.0000x reference)
; #define GAS __attribute__((address_space(1)))
; #define LAS __attribute__((address_space(3)))
; #define KARG_IN(kp, i) (*(const float* const __attribute__((address_space(4)))*)((kp) + 8 * (i)))
; __device__ __forceinline__ void p0_fold_tile(const float* keys_l, const float* wq_l, bf16* WT, int tile, int lane, LAS float* scr  ) {
;     ...
;     const int db = tile & 31, kb = (tile >> 5) & 3, hc = tile >> 7, r = lane & 31, kh = lane >> 5;
;     LAS float* sa = scr; LAS float* sb = scr + 32 * 64;
;     const int lr = lane >> 4, lc = (lane & 15) * 4;
;     const GAS float* ag = (const GAS float*)keys_l + ((size_t)hc * 128 + kb * 32) * 128;
;     const GAS float* bg = (const GAS float*)wq_l + (size_t)(db * 32) * NPQ + hc * 128;
;     f32x16 acc;
; #pragma unroll
;     for (int i = 0; i < 16; ++i) acc[i] = 0.f;
; #pragma unroll 1
;     for (int h = 0; h < 2; ++h) {
;         f32x4 va[8], vb[8];
; #pragma unroll
;         for (int q = 0; q < 8; ++q) { va[q] = *(const GAS f32x4*)(ag + (size_t)(4 * q + lr) * 128 + h * 64 + lc); vb[q] = *(const GAS f32x4*)(bg + (size_t)(4 * q + lr) * NPQ + h * 64 + lc); }
; #pragma unroll
;         for (int q = 0; q < 8; ++q) { const int row = 4 * q + lr, gsw = (((lane & 15) ^ (row & 15)) << 2); *(LAS f32x4*)(sa + row * 64 + gsw) = va[q]; *(LAS f32x4*)(sb + row * 64 + gsw) = vb[q]; }
; __global__ void __launch_bounds__(NWAVES * 64, 2) mega(Args args) {
;     ...
;         for (int repf = 0; repf < MK_REP_FOLD; ++repf)
;         for (int it = gw; it < 2 * 2048; it += NGW) { const int l = it >> 11;
;             p0_fold_tile(KARG_IN(kp, 10) + (size_t)l * 16 * 128 * 128, KARG_IN(kp, 9) + (size_t)l * D * NPQ, (bf16*)(ws + WS_WQ) + (size_t)l * NPQ * D, it & 2047, F.lane, scr); }
.LBB0_35:
	s_cmpk_lt_i32 s8, 0x1000
	s_cbranch_scc0 .LBB0_40
	v_lshrrev_b32_e32 v3, 4, v58
	v_xor_b32_e32 v15, v3, v0
	v_lshlrev_b32_e32 v15, 4, v15
	v_lshlrev_b32_e32 v16, 8, v3
	v_and_b32_e32 v15, 0xf0, v15
	v_add3_u32 v59, s9, v16, v15
	v_bitop3_b32 v16, v3, v0, 4 bitop3:0x36
	v_or_b32_e32 v8, 4, v3
	v_lshlrev_b32_e32 v16, 4, v16
	v_lshlrev_b32_e32 v24, 9, v8
	v_lshlrev_b32_e32 v26, 13, v8
	v_lshlrev_b32_e32 v8, 8, v8
	v_and_b32_e32 v16, 0xf0, v16
	v_add3_u32 v60, s9, v8, v16
	v_bitop3_b32 v8, v3, v0, 8 bitop3:0x36
	v_or_b32_e32 v9, 8, v3
	v_lshlrev_b32_e32 v8, 4, v8
	v_lshlrev_b32_e32 v28, 9, v9
	v_lshlrev_b32_e32 v30, 13, v9
	v_lshlrev_b32_e32 v9, 8, v9
	v_and_b32_e32 v8, 0xf0, v8
	v_add3_u32 v61, s9, v9, v8
	v_bitop3_b32 v8, v3, v0, 12 bitop3:0x36
	v_or_b32_e32 v10, 12, v3
	v_lshlrev_b32_e32 v8, 4, v8
	v_or_b32_e32 v11, 16, v3
	v_lshlrev_b32_e32 v9, 8, v10
	v_and_b32_e32 v8, 0xf0, v8
	v_add3_u32 v62, s9, v9, v8
	v_lshlrev_b32_e32 v8, 8, v11
	v_add3_u32 v63, s9, v8, v15
	v_bitop3_b32 v8, v3, v0, 20 bitop3:0x36
	v_or_b32_e32 v12, 20, v3
	v_lshlrev_b32_e32 v8, 4, v8
	v_lshlrev_b32_e32 v9, 8, v12
	v_and_b32_e32 v8, 0xf0, v8
	v_add3_u32 v64, s9, v9, v8
	v_bitop3_b32 v8, v3, v0, 24 bitop3:0x36
	v_lshlrev_b32_e32 v20, 9, v3
	v_lshlrev_b32_e32 v22, 13, v3
	v_or_b32_e32 v13, 24, v3
	v_or_b32_e32 v14, 28, v3
	v_lshlrev_b32_e32 v8, 4, v8
	v_bitop3_b32 v3, v3, v0, 28 bitop3:0x36
	v_lshlrev_b32_e32 v9, 8, v13
	v_and_b32_e32 v8, 0xf0, v8
	v_lshlrev_b32_e32 v3, 4, v3
	v_lshlrev_b32_e32 v4, 3, v6
	v_add3_u32 v65, s9, v9, v8
	v_lshlrev_b32_e32 v8, 8, v14
	v_and_b32_e32 v3, 0xf0, v3
	v_and_b32_e32 v5, 15, v0
	v_lshl_add_u32 v7, v1, 8, s9
	v_add3_u32 v66, s9, v8, v3
	v_bitop3_b32 v3, v4, v0, 15 bitop3:0x78
	v_lshl_add_u32 v67, v3, 4, v7
	v_bitop3_b32 v3, v4, v5, 1 bitop3:0x36
	v_lshl_add_u32 v68, v3, 4, v7
	v_bitop3_b32 v3, v4, v5, 2 bitop3:0x36
	v_lshl_add_u32 v69, v3, 4, v7
	v_bitop3_b32 v3, v4, v5, 3 bitop3:0x36
	v_lshl_add_u32 v70, v3, 4, v7
	v_bitop3_b32 v3, v4, v5, 4 bitop3:0x36
	v_lshl_add_u32 v71, v3, 4, v7
	v_bitop3_b32 v3, v4, v5, 5 bitop3:0x36
	v_mov_b32_e32 v19, 0
	v_lshl_add_u32 v72, v3, 4, v7
	v_bitop3_b32 v3, v4, v5, 6 bitop3:0x36
	v_lshlrev_b32_e32 v18, 1, v1
	v_lshl_add_u32 v73, v3, 4, v7
	v_bitop3_b32 v3, v4, v5, 7 bitop3:0x36
	v_lshl_add_u64 v[4:5], s[30:31], 0, v[18:19]
	s_mov_b64 s[4:5], 0x1000000
	v_lshl_add_u64 v[52:53], v[4:5], 0, s[4:5]
	s_load_dwordx4 s[4:7], s[10:11], 0x48
	v_lshlrev_b32_e32 v2, 2, v0
	v_and_b32_e32 v2, 60, v2
	v_mov_b32_e32 v21, v19
	v_mov_b32_e32 v23, v19
	v_mov_b32_e32 v25, v19
	v_mov_b32_e32 v27, v19
	v_mov_b32_e32 v29, v19
	v_mov_b32_e32 v31, v19
	v_lshlrev_b32_e32 v32, 9, v10
	v_mov_b32_e32 v33, v19
	v_lshlrev_b32_e32 v34, 13, v10
	v_mov_b32_e32 v35, v19
	v_lshlrev_b32_e32 v36, 9, v11
	v_mov_b32_e32 v37, v19
	v_lshlrev_b32_e32 v38, 13, v11
	v_mov_b32_e32 v39, v19
	v_lshlrev_b32_e32 v40, 9, v12
	v_mov_b32_e32 v41, v19
	v_lshlrev_b32_e32 v42, 13, v12
	v_mov_b32_e32 v43, v19
	v_lshlrev_b32_e32 v44, 9, v13
	v_mov_b32_e32 v45, v19
	v_lshlrev_b32_e32 v46, 13, v13
	v_mov_b32_e32 v47, v19
	v_lshlrev_b32_e32 v48, 9, v14
	v_mov_b32_e32 v49, v19
	v_lshlrev_b32_e32 v50, 13, v14
	v_mov_b32_e32 v51, v19
	v_lshl_add_u32 v74, v3, 4, v7
	v_lshlrev_b32_e32 v75, 2, v6
	s_mov_b32 s13, 0
	v_lshlrev_b32_e32 v18, 2, v2
	s_movk_i32 s9, 0x7fff
	s_mov_b32 s20, s8
	.p2align 7

;     __device__ __forceinline__ bool next(int i, Unit& u) const { return i == 0 && b.next(round, u); }
;   __device__ __forceinline__ bool next(int i,AttnUnit&u)const{ if(i>=2)return false; const int j=vcu&31,s=j&15; u.bh=(vcu>>5)*4+(j>>4)*2+i; u.qb=(i==0)?s:15-s; return true; }
; template <class Epi, class Sched, bool ALIGN_EPI = false, bool SP2 = false>
; __device__ __forceinline__ void gemm_phase(int wave_id  , PG8_LAS unsigned char* lds, const Gemm g, const Sched& S, const Epi& E) {
;     ...
;     for (;;) {
;         const bool has_next = S.next(ui + 1, nxt);
;         const char* nA = has_next ? (const char*)g.A + (size_t)nxt.pm * tstep : cA; const char* nB = has_next ? (const char*)g.Bt + (size_t)nxt.pn * tstep : cB;
;         for (int t = 0; t < nt; t += 2) {
.LBB0_120:
	s_andn2_b64 vcc, exec, s[6:7]
	s_mov_b32 s48, s26
	s_mov_b32 s14, s28
	s_mov_b64 s[8:9], s[44:45]
	s_mov_b64 s[46:47], s[42:43]
	s_cbranch_vccz .LBB0_175
	.p2align 7

; #define PG8_STAGE(bufoff, gbase, voff) do { _Pragma("unroll") for (int _i = 0; _i < 2; ++_i) \
;         __builtin_amdgcn_global_load_lds((const unsigned*)((const char*)(gbase) + (voff)[_i]), (PG8_LAS unsigned*)(lds + (bufoff) + ldsw + _i * 8192), 16, 0, 0); } while (0)
; #define PG8_WAIT_V(n) asm volatile("s_waitcnt vmcnt(" #n ")" ::: "memory")
; #define PG8_BAR __builtin_amdgcn_s_barrier()
; template <class Epi, class Sched, bool ALIGN_EPI = false, bool SP2 = false>
; __device__ __forceinline__ void gemm_phase(int wave_id  , PG8_LAS unsigned char* lds, const Gemm g, const Sched& S, const Epi& E) {
;     ...
;     f32x4 acc[2][2][4][2];
; #pragma unroll
;     for (int a = 0; a < 2; ++a)
; #pragma unroll
;         for (int b = 0; b < 2; ++b)
; #pragma unroll
;             for (int m = 0; m < 4; ++m)
; #pragma unroll
;                 for (int n = 0; n < 2; ++n) acc[a][b][m][n] = (f32x4){0.f, 0.f, 0.f, 0.f};
;     bf16x8 At[4][2], B0[2][2], B1[2][2];
;     const char* cA = (const char*)g.A + (size_t)cur.pm * tstep; const char* cB = (const char*)g.Bt + (size_t)cur.pn * tstep;
;     S.a_ready(cur);
;     if constexpr (SP2) {
;         PG8_STAGE(PG8_SB(0, 0), cB, voffB); PG8_STAGE(PG8_SB(0, 1), cB + hstep, voffB); PG8_STAGE(PG8_SA(0, 0), cA, voffA); PG8_STAGE(PG8_SA(0, 1), cA + hstep, voffA);
;         if (wr == 1) PG8_BAR;
;         PG8_WAIT_V(2); PG8_BAR;
;         PG8_STAGE(PG8_SB(1, 0), cB + kstep, voffB); PG8_STAGE(PG8_SA(1, 0), cA + kstep, voffA); PG8_STAGE(PG8_SB(1, 1), cB + hstep + kstep, voffB);
;         PG8_WAIT_V(6); PG8_BAR;
.LBB0_437:
	v_and_b32_e32 v145, 15, v144
	v_and_b32_e32 v14, 48, v144
	v_lshlrev_b32_e32 v15, 2, v144
	s_mov_b64 s[20:21], 0x80
	s_sext_i32_i8 s8, s4
	s_and_b32 s17, s48, 3
	s_lshl_b32 s4, s9, 13
	v_lshl_or_b32 v14, v145, 6, v14
	v_and_b32_e32 v15, 32, v15
	s_add_i32 m0, s56, 0x18000
	v_lshl_add_u64 v[6:7], v[6:7], 0, s[20:21]
	s_lshl_b32 s57, s9, 6
	v_bitop3_b32 v16, v14, s4, v15 bitop3:0xde
	s_lshl_b32 s4, s17, 12
	s_waitcnt vmcnt(2)
	s_barrier
	global_load_lds_dwordx4 v[6:7], off
	v_lshl_add_u64 v[4:5], v[4:5], 0, s[20:21]
	s_add_i32 m0, s56, 0x1a000
	s_add_i32 s65, s56, 0x8000
	s_add_i32 s66, s56, 0xa000
	global_load_lds_dwordx4 v[4:5], off
	v_lshl_add_u64 v[2:3], v[2:3], 0, s[20:21]
	s_mov_b32 m0, s65
	s_add_u32 s6, s42, 0x40080
	global_load_lds_dwordx4 v[2:3], off
	v_lshl_add_u64 v[0:1], v[0:1], 0, s[20:21]
	s_mov_b32 m0, s66
	s_addc_u32 s7, s43, 0
	global_load_lds_dwordx4 v[0:1], off
	s_add_i32 m0, s56, 0x1c000
	v_lshl_add_u64 v[0:1], s[6:7], 0, v[128:129]
	global_load_lds_dwordx4 v[0:1], off
	v_lshl_add_u64 v[0:1], s[6:7], 0, v[130:131]
	s_add_i32 m0, s56, 0x1e000
	v_bitop3_b32 v146, v14, s4, v15 bitop3:0xde
	global_load_lds_dwordx4 v[0:1], off
	v_lshlrev_b32_e32 v0, 14, v8
	v_and_b32_e32 v0, 0xffff8000, v0
	v_lshl_add_u32 v0, v9, 11, v0
	v_and_b32_e32 v1, 1, v8
	v_lshl_or_b32 v0, v1, 6, v0
	s_mov_b64 s[4:5], 0x40080
	v_lshl_add_u32 v0, v10, 1, v0
	v_mov_b32_e32 v1, 0
	v_lshl_add_u64 v[132:133], v[0:1], 0, s[4:5]
	v_lshlrev_b32_e32 v0, 14, v11
	v_and_b32_e32 v0, 0xffff8000, v0
	v_lshl_add_u32 v0, v12, 11, v0
	v_and_b32_e32 v2, 1, v11
	s_waitcnt vmcnt(6)
	v_lshl_or_b32 v0, v2, 6, v0
	v_lshl_add_u32 v0, v13, 1, v0
	v_or_b32_e32 v160, s57, v145
	s_mov_b32 s64, 0
	v_lshl_add_u64 v[134:135], v[0:1], 0, s[4:5]
	v_mov_b64_e32 v[136:137], 0x100
	v_mov_b64_e32 v[138:139], 0xff
	s_add_i32 s67, 0, 0x10000
	s_add_i32 s68, 0, 0x14000
	v_add_u32_e32 v147, 0, v16
	v_mov_b32_e32 v0, v1
	v_mov_b32_e32 v2, v1
	v_mov_b32_e32 v3, v1
	v_mov_b32_e32 v4, v1
	v_mov_b32_e32 v5, v1
	v_mov_b32_e32 v6, v1
	v_mov_b32_e32 v7, v1
	v_mov_b32_e32 v16, v1
	v_mov_b32_e32 v17, v1
	v_mov_b32_e32 v18, v1
	v_mov_b32_e32 v19, v1
	v_mov_b32_e32 v20, v1
	v_mov_b32_e32 v21, v1
	v_mov_b32_e32 v22, v1
	v_mov_b32_e32 v23, v1
	v_mov_b32_e32 v32, v1
	v_mov_b32_e32 v33, v1
	v_mov_b32_e32 v34, v1
	v_mov_b32_e32 v35, v1
	v_mov_b32_e32 v40, v1
	v_mov_b32_e32 v41, v1
	v_mov_b32_e32 v42, v1
	v_mov_b32_e32 v43, v1
	v_mov_b32_e32 v36, v1
	v_mov_b32_e32 v37, v1
	v_mov_b32_e32 v38, v1
	v_mov_b32_e32 v39, v1
	v_mov_b32_e32 v44, v1
	v_mov_b32_e32 v45, v1
	v_mov_b32_e32 v46, v1
	v_mov_b32_e32 v47, v1
	v_mov_b32_e32 v8, v1
	v_mov_b32_e32 v9, v1
	v_mov_b32_e32 v10, v1
	v_mov_b32_e32 v11, v1
	v_mov_b32_e32 v12, v1
	v_mov_b32_e32 v13, v1
	v_mov_b32_e32 v14, v1
	v_mov_b32_e32 v15, v1
	v_mov_b32_e32 v24, v1
	v_mov_b32_e32 v25, v1
	v_mov_b32_e32 v26, v1
	v_mov_b32_e32 v27, v1
	v_mov_b32_e32 v28, v1
	v_mov_b32_e32 v29, v1
	v_mov_b32_e32 v30, v1
	v_mov_b32_e32 v31, v1
	v_mov_b32_e32 v48, v1
	v_mov_b32_e32 v49, v1
	v_mov_b32_e32 v50, v1
	v_mov_b32_e32 v51, v1
	v_mov_b32_e32 v56, v1
	v_mov_b32_e32 v57, v1
	v_mov_b32_e32 v58, v1
	v_mov_b32_e32 v59, v1
	v_mov_b32_e32 v52, v1
	v_mov_b32_e32 v53, v1
	v_mov_b32_e32 v54, v1
	v_mov_b32_e32 v55, v1
	v_mov_b32_e32 v60, v1
	v_mov_b32_e32 v61, v1
	v_mov_b32_e32 v62, v1
	v_mov_b32_e32 v63, v1
	v_mov_b32_e32 v64, v1
	v_mov_b32_e32 v65, v1
	v_mov_b32_e32 v66, v1
	v_mov_b32_e32 v67, v1
	v_mov_b32_e32 v72, v1
	v_mov_b32_e32 v73, v1
	v_mov_b32_e32 v74, v1
	v_mov_b32_e32 v75, v1
	v_mov_b32_e32 v68, v1
	v_mov_b32_e32 v69, v1
	v_mov_b32_e32 v70, v1
	v_mov_b32_e32 v71, v1
	v_mov_b32_e32 v80, v1
	v_mov_b32_e32 v81, v1
	v_mov_b32_e32 v82, v1
	v_mov_b32_e32 v83, v1
	v_mov_b32_e32 v76, v1
	v_mov_b32_e32 v77, v1
	v_mov_b32_e32 v78, v1
	v_mov_b32_e32 v79, v1
	v_mov_b32_e32 v88, v1
	v_mov_b32_e32 v89, v1
	v_mov_b32_e32 v90, v1
	v_mov_b32_e32 v91, v1
	v_mov_b32_e32 v100, v1
	v_mov_b32_e32 v101, v1
	v_mov_b32_e32 v102, v1
	v_mov_b32_e32 v103, v1
	v_mov_b32_e32 v116, v1
	v_mov_b32_e32 v117, v1
	v_mov_b32_e32 v118, v1
	v_mov_b32_e32 v119, v1
	v_mov_b32_e32 v84, v1
	v_mov_b32_e32 v85, v1
	v_mov_b32_e32 v86, v1
	v_mov_b32_e32 v87, v1
	v_mov_b32_e32 v96, v1
	v_mov_b32_e32 v97, v1
	v_mov_b32_e32 v98, v1
	v_mov_b32_e32 v99, v1
	v_mov_b32_e32 v92, v1
	v_mov_b32_e32 v93, v1
	v_mov_b32_e32 v94, v1
	v_mov_b32_e32 v95, v1
	v_mov_b32_e32 v108, v1
	v_mov_b32_e32 v109, v1
	v_mov_b32_e32 v110, v1
	v_mov_b32_e32 v111, v1
	v_mov_b32_e32 v104, v1
	v_mov_b32_e32 v105, v1
	v_mov_b32_e32 v106, v1
	v_mov_b32_e32 v107, v1
	v_mov_b32_e32 v112, v1
	v_mov_b32_e32 v113, v1
	v_mov_b32_e32 v114, v1
	v_mov_b32_e32 v115, v1
	v_mov_b32_e32 v120, v1
	v_mov_b32_e32 v121, v1
	v_mov_b32_e32 v122, v1
	v_mov_b32_e32 v123, v1
	v_mov_b32_e32 v124, v1
	v_mov_b32_e32 v125, v1
	v_mov_b32_e32 v126, v1
	v_mov_b32_e32 v127, v1
	s_barrier
	.p2align 7

; #define PG8_STAGE(bufoff, gbase, voff) do { _Pragma("unroll") for (int _i = 0; _i < 2; ++_i) \
;         __builtin_amdgcn_global_load_lds((const unsigned*)((const char*)(gbase) + (voff)[_i]), (PG8_LAS unsigned*)(lds + (bufoff) + ldsw + _i * 8192), 16, 0, 0); } while (0)
; #define PG8_WAIT_V(n) asm volatile("s_waitcnt vmcnt(" #n ")" ::: "memory")
; #define PG8_BAR __builtin_amdgcn_s_barrier()
; template <class Epi, class Sched, bool ALIGN_EPI = false, bool SP2 = false>
; __device__ __forceinline__ void gemm_phase(int wave_id  , PG8_LAS unsigned char* lds, const Gemm g, const Sched& S, const Epi& E) {
;     ...
;     f32x4 acc[2][2][4][2];
; #pragma unroll
;     for (int a = 0; a < 2; ++a)
; #pragma unroll
;         for (int b = 0; b < 2; ++b)
; #pragma unroll
;             for (int m = 0; m < 4; ++m)
; #pragma unroll
;                 for (int n = 0; n < 2; ++n) acc[a][b][m][n] = (f32x4){0.f, 0.f, 0.f, 0.f};
;     bf16x8 At[4][2], B0[2][2], B1[2][2];
;     const char* cA = (const char*)g.A + (size_t)cur.pm * tstep; const char* cB = (const char*)g.Bt + (size_t)cur.pn * tstep;
;     S.a_ready(cur);
;     if constexpr (SP2) {
;         PG8_STAGE(PG8_SB(0, 0), cB, voffB); PG8_STAGE(PG8_SB(0, 1), cB + hstep, voffB); PG8_STAGE(PG8_SA(0, 0), cA, voffA); PG8_STAGE(PG8_SA(0, 1), cA + hstep, voffA);
;         if (wr == 1) PG8_BAR;
;         PG8_WAIT_V(2); PG8_BAR;
;         PG8_STAGE(PG8_SB(1, 0), cB + kstep, voffB); PG8_STAGE(PG8_SA(1, 0), cA + kstep, voffA); PG8_STAGE(PG8_SB(1, 1), cB + hstep + kstep, voffB);
;         PG8_WAIT_V(6); PG8_BAR;
.LBB0_576:
	v_and_b32_e32 v138, 15, v139
	v_and_b32_e32 v14, 48, v139
	v_lshlrev_b32_e32 v15, 2, v139
	s_and_b32 s57, s51, 3
	v_lshl_or_b32 v14, v138, 6, v14
	s_lshl_b32 s24, s52, 13
	v_and_b32_e32 v15, 32, v15
	v_bitop3_b32 v16, v14, s24, v15 bitop3:0xde
	s_lshl_b32 s24, s57, 12
	v_bitop3_b32 v14, v14, s24, v15 bitop3:0xde
	s_mov_b64 s[24:25], 0x80
	s_add_i32 m0, s19, 0x18000
	v_lshl_add_u64 v[6:7], v[6:7], 0, s[24:25]
	s_waitcnt vmcnt(2)
	s_barrier
	global_load_lds_dwordx4 v[6:7], off
	v_lshl_add_u64 v[4:5], v[4:5], 0, s[24:25]
	s_add_i32 m0, s19, 0x1a000
	s_add_i32 s58, s19, 0x8000
	s_add_i32 s59, s19, 0xa000
	global_load_lds_dwordx4 v[4:5], off
	v_lshl_add_u64 v[0:1], v[0:1], 0, s[24:25]
	s_mov_b32 m0, s58
	s_add_u32 s34, s4, 0x40080
	global_load_lds_dwordx4 v[0:1], off
	v_lshl_add_u64 v[0:1], v[2:3], 0, s[24:25]
	s_mov_b32 m0, s59
	s_addc_u32 s35, s5, 0
	global_load_lds_dwordx4 v[0:1], off
	s_add_i32 m0, s19, 0x1c000
	v_lshl_add_u64 v[0:1], s[34:35], 0, v[130:131]
	global_load_lds_dwordx4 v[0:1], off
	v_lshl_add_u64 v[0:1], s[34:35], 0, v[128:129]
	s_add_i32 m0, s19, 0x1e000
	s_add_u32 s26, s14, s26
	global_load_lds_dwordx4 v[0:1], off
	s_addc_u32 s27, s15, s27
	s_add_u32 s62, s26, 0x1000100
	s_addc_u32 s63, s27, 0
	s_sub_i32 s26, s28, s44
	s_lshl_b32 s27, s43, 5
	s_sub_i32 s26, s26, s27
	s_sext_i32_i8 s26, s26
	s_add_i32 s26, s29, s26
	v_lshlrev_b32_e32 v0, 14, v8
	s_ashr_i32 s27, s26, 31
	v_and_b32_e32 v0, 0xffff8000, v0
	s_lshl_b64 s[26:27], s[26:27], 19
	v_lshl_add_u32 v0, v10, 11, v0
	v_and_b32_e32 v1, 1, v8
	v_lshl_or_b32 v0, v1, 6, v0
	s_add_u32 s26, s14, s26
	v_lshl_add_u32 v0, v11, 1, v0
	v_mov_b32_e32 v1, v131
	s_addc_u32 s27, s15, s27
	v_lshl_add_u64 v[0:1], s[26:27], 0, v[0:1]
	s_mov_b64 s[28:29], 0x6040080
	v_lshl_add_u64 v[132:133], v[0:1], 0, s[28:29]
	v_lshlrev_b32_e32 v0, 14, v9
	v_and_b32_e32 v0, 0xffff8000, v0
	v_lshl_add_u32 v0, v12, 11, v0
	v_and_b32_e32 v1, 1, v9
	v_lshl_or_b32 v0, v1, 6, v0
	s_waitcnt vmcnt(6)
	v_lshl_add_u32 v0, v13, 1, v0
	v_mov_b32_e32 v1, v131
	s_add_i32 s67, 0, 0x10000
	s_add_i32 s69, 0, 0x14000
	s_add_i32 s71, 0, 0x18000
	s_add_i32 s73, 0, 0x1c000
	v_lshl_add_u64 v[0:1], s[26:27], 0, v[0:1]
	v_add_u32_e32 v140, s67, v14
	v_add_u32_e32 v141, s69, v14
	s_add_i32 s67, s67, s42
	s_add_i32 s69, s69, s42
	v_add_u32_e32 v143, s71, v14
	v_add_u32_e32 v144, s73, v14
	s_add_i32 s71, s71, s42
	s_add_i32 s73, s73, s42
	v_lshl_add_u64 v[134:135], v[0:1], 0, s[28:29]
	s_mov_b32 s64, -2
	s_mov_b64 s[28:29], 0
	v_add_u32_e32 v142, 0, v16
	s_add_i32 s65, s19, 0xc000
	s_add_i32 s66, s19, 0xe000
	s_add_i32 s68, s67, 0x2000
	s_add_i32 s70, s69, 0x2000
	s_add_i32 s72, s71, 0x2000
	s_add_i32 s74, s73, 0x2000
	v_mov_b32_e32 v0, v131
	v_mov_b32_e32 v1, v131
	v_mov_b32_e32 v2, v131
	v_mov_b32_e32 v3, v131
	v_mov_b32_e32 v4, v131
	v_mov_b32_e32 v5, v131
	v_mov_b32_e32 v6, v131
	v_mov_b32_e32 v7, v131
	v_mov_b32_e32 v8, v131
	v_mov_b32_e32 v9, v131
	v_mov_b32_e32 v10, v131
	v_mov_b32_e32 v11, v131
	v_mov_b32_e32 v12, v131
	v_mov_b32_e32 v13, v131
	v_mov_b32_e32 v14, v131
	v_mov_b32_e32 v15, v131
	v_mov_b32_e32 v16, v131
	v_mov_b32_e32 v17, v131
	v_mov_b32_e32 v18, v131
	v_mov_b32_e32 v19, v131
	v_mov_b32_e32 v20, v131
	v_mov_b32_e32 v21, v131
	v_mov_b32_e32 v22, v131
	v_mov_b32_e32 v23, v131
	v_mov_b32_e32 v24, v131
	v_mov_b32_e32 v25, v131
	v_mov_b32_e32 v26, v131
	v_mov_b32_e32 v27, v131
	v_mov_b32_e32 v28, v131
	v_mov_b32_e32 v29, v131
	v_mov_b32_e32 v30, v131
	v_mov_b32_e32 v31, v131
	v_mov_b32_e32 v64, v131
	v_mov_b32_e32 v65, v131
	v_mov_b32_e32 v66, v131
	v_mov_b32_e32 v67, v131
	v_mov_b32_e32 v68, v131
	v_mov_b32_e32 v69, v131
	v_mov_b32_e32 v70, v131
	v_mov_b32_e32 v71, v131
	v_mov_b32_e32 v72, v131
	v_mov_b32_e32 v73, v131
	v_mov_b32_e32 v74, v131
	v_mov_b32_e32 v75, v131
	v_mov_b32_e32 v76, v131
	v_mov_b32_e32 v77, v131
	v_mov_b32_e32 v78, v131
	v_mov_b32_e32 v79, v131
	v_mov_b32_e32 v80, v131
	v_mov_b32_e32 v81, v131
	v_mov_b32_e32 v82, v131
	v_mov_b32_e32 v83, v131
	v_mov_b32_e32 v84, v131
	v_mov_b32_e32 v85, v131
	v_mov_b32_e32 v86, v131
	v_mov_b32_e32 v87, v131
	v_mov_b32_e32 v88, v131
	v_mov_b32_e32 v89, v131
	v_mov_b32_e32 v90, v131
	v_mov_b32_e32 v91, v131
	v_mov_b32_e32 v92, v131
	v_mov_b32_e32 v93, v131
	v_mov_b32_e32 v94, v131
	v_mov_b32_e32 v95, v131
	v_mov_b32_e32 v32, v131
	v_mov_b32_e32 v33, v131
	v_mov_b32_e32 v34, v131
	v_mov_b32_e32 v35, v131
	v_mov_b32_e32 v36, v131
	v_mov_b32_e32 v37, v131
	v_mov_b32_e32 v38, v131
	v_mov_b32_e32 v39, v131
	v_mov_b32_e32 v40, v131
	v_mov_b32_e32 v41, v131
	v_mov_b32_e32 v42, v131
	v_mov_b32_e32 v43, v131
	v_mov_b32_e32 v44, v131
	v_mov_b32_e32 v45, v131
	v_mov_b32_e32 v46, v131
	v_mov_b32_e32 v47, v131
	v_mov_b32_e32 v48, v131
	v_mov_b32_e32 v49, v131
	v_mov_b32_e32 v50, v131
	v_mov_b32_e32 v51, v131
	v_mov_b32_e32 v52, v131
	v_mov_b32_e32 v53, v131
	v_mov_b32_e32 v54, v131
	v_mov_b32_e32 v55, v131
	v_mov_b32_e32 v56, v131
	v_mov_b32_e32 v57, v131
	v_mov_b32_e32 v58, v131
	v_mov_b32_e32 v59, v131
	v_mov_b32_e32 v60, v131
	v_mov_b32_e32 v61, v131
	v_mov_b32_e32 v62, v131
	v_mov_b32_e32 v63, v131
	v_mov_b32_e32 v96, v131
	v_mov_b32_e32 v97, v131
	v_mov_b32_e32 v98, v131
	v_mov_b32_e32 v99, v131
	v_mov_b32_e32 v100, v131
	v_mov_b32_e32 v101, v131
	v_mov_b32_e32 v102, v131
	v_mov_b32_e32 v103, v131
	v_mov_b32_e32 v104, v131
	v_mov_b32_e32 v105, v131
	v_mov_b32_e32 v106, v131
	v_mov_b32_e32 v107, v131
	v_mov_b32_e32 v108, v131
	v_mov_b32_e32 v109, v131
	v_mov_b32_e32 v110, v131
	v_mov_b32_e32 v111, v131
	v_mov_b32_e32 v112, v131
	v_mov_b32_e32 v113, v131
	v_mov_b32_e32 v114, v131
	v_mov_b32_e32 v115, v131
	v_mov_b32_e32 v116, v131
	v_mov_b32_e32 v117, v131
	v_mov_b32_e32 v118, v131
	v_mov_b32_e32 v119, v131
	v_mov_b32_e32 v120, v131
	v_mov_b32_e32 v121, v131
	v_mov_b32_e32 v122, v131
	v_mov_b32_e32 v123, v131
	v_mov_b32_e32 v124, v131
	v_mov_b32_e32 v125, v131
	v_mov_b32_e32 v126, v131
	v_mov_b32_e32 v127, v131
	s_barrier
	.p2align 7

; #define PG8_STAGE(bufoff, gbase, voff) do { _Pragma("unroll") for (int _i = 0; _i < 2; ++_i) \
;         __builtin_amdgcn_global_load_lds((const unsigned*)((const char*)(gbase) + (voff)[_i]), (PG8_LAS unsigned*)(lds + (bufoff) + ldsw + _i * 8192), 16, 0, 0); } while (0)
; #define PG8_WAIT_V(n) asm volatile("s_waitcnt vmcnt(" #n ")" ::: "memory")
; #define PG8_BAR __builtin_amdgcn_s_barrier()
; template <class Epi, class Sched, bool ALIGN_EPI = false, bool SP2 = false>
; __device__ __forceinline__ void gemm_phase(int wave_id  , PG8_LAS unsigned char* lds, const Gemm g, const Sched& S, const Epi& E) {
;     ...
;     f32x4 acc[2][2][4][2];
; #pragma unroll
;     for (int a = 0; a < 2; ++a)
; #pragma unroll
;         for (int b = 0; b < 2; ++b)
; #pragma unroll
;             for (int m = 0; m < 4; ++m)
; #pragma unroll
;                 for (int n = 0; n < 2; ++n) acc[a][b][m][n] = (f32x4){0.f, 0.f, 0.f, 0.f};
;     bf16x8 At[4][2], B0[2][2], B1[2][2];
;     const char* cA = (const char*)g.A + (size_t)cur.pm * tstep; const char* cB = (const char*)g.Bt + (size_t)cur.pn * tstep;
;     S.a_ready(cur);
;     if constexpr (SP2) {
;         PG8_STAGE(PG8_SB(0, 0), cB, voffB); PG8_STAGE(PG8_SB(0, 1), cB + hstep, voffB); PG8_STAGE(PG8_SA(0, 0), cA, voffA); PG8_STAGE(PG8_SA(0, 1), cA + hstep, voffA);
;         if (wr == 1) PG8_BAR;
;         PG8_WAIT_V(2); PG8_BAR;
;         PG8_STAGE(PG8_SB(1, 0), cB + kstep, voffB); PG8_STAGE(PG8_SA(1, 0), cA + kstep, voffA); PG8_STAGE(PG8_SB(1, 1), cB + hstep + kstep, voffB);
;         PG8_WAIT_V(6); PG8_BAR;
.LBB0_594:
	v_and_b32_e32 v138, 15, v137
	v_and_b32_e32 v14, 48, v137
	v_lshlrev_b32_e32 v15, 2, v137
	s_and_b32 s48, s44, 3
	v_lshl_or_b32 v14, v138, 6, v14
	s_lshl_b32 s24, s45, 13
	v_and_b32_e32 v15, 32, v15
	v_bitop3_b32 v16, v14, s24, v15 bitop3:0xde
	s_lshl_b32 s24, s48, 12
	v_bitop3_b32 v14, v14, s24, v15 bitop3:0xde
	s_mov_b64 s[24:25], 0x80
	s_add_i32 m0, s19, 0x18000
	v_lshl_add_u64 v[6:7], v[6:7], 0, s[24:25]
	s_waitcnt vmcnt(2)
	s_barrier
	global_load_lds_dwordx4 v[6:7], off
	v_lshl_add_u64 v[4:5], v[4:5], 0, s[24:25]
	s_add_i32 m0, s19, 0x1a000
	s_add_i32 s50, s19, 0x8000
	s_add_i32 s51, s19, 0xa000
	global_load_lds_dwordx4 v[4:5], off
	v_lshl_add_u64 v[0:1], v[0:1], 0, s[24:25]
	s_mov_b32 m0, s50
	s_add_u32 s34, s4, 0x40080
	global_load_lds_dwordx4 v[0:1], off
	v_lshl_add_u64 v[0:1], v[2:3], 0, s[24:25]
	s_mov_b32 m0, s51
	s_addc_u32 s35, s5, 0
	global_load_lds_dwordx4 v[0:1], off
	s_add_i32 m0, s19, 0x1c000
	v_lshl_add_u64 v[0:1], s[34:35], 0, v[130:131]
	global_load_lds_dwordx4 v[0:1], off
	v_lshl_add_u64 v[0:1], s[34:35], 0, v[128:129]
	s_add_i32 m0, s19, 0x1e000
	s_add_u32 s28, s14, s28
	global_load_lds_dwordx4 v[0:1], off
	s_addc_u32 s29, s15, s29
	v_lshlrev_b32_e32 v0, 14, v8
	s_add_u32 s52, s28, 0x1000100
	v_and_b32_e32 v0, 0xffff8000, v0
	s_addc_u32 s53, s29, 0
	v_lshl_add_u32 v0, v10, 11, v0
	v_and_b32_e32 v1, 1, v8
	v_lshl_or_b32 v0, v1, 6, v0
	s_add_u32 s14, s14, s26
	v_lshl_add_u32 v0, v11, 1, v0
	v_mov_b32_e32 v1, v131
	s_addc_u32 s15, s15, s27
	v_lshl_add_u64 v[0:1], s[14:15], 0, v[0:1]
	s_mov_b64 s[26:27], 0x6040080
	v_lshl_add_u64 v[132:133], v[0:1], 0, s[26:27]
	v_lshlrev_b32_e32 v0, 14, v9
	v_and_b32_e32 v0, 0xffff8000, v0
	v_lshl_add_u32 v0, v12, 11, v0
	v_and_b32_e32 v1, 1, v9
	v_lshl_or_b32 v0, v1, 6, v0
	s_waitcnt vmcnt(6)
	v_lshl_add_u32 v0, v13, 1, v0
	v_mov_b32_e32 v1, v131
	s_add_i32 s57, 0, 0x10000
	s_add_i32 s59, 0, 0x14000
	s_add_i32 s63, 0, 0x18000
	s_add_i32 s65, 0, 0x1c000
	v_lshl_add_u64 v[0:1], s[14:15], 0, v[0:1]
	v_add_u32_e32 v139, s57, v14
	v_add_u32_e32 v140, s59, v14
	s_add_i32 s57, s57, s42
	s_add_i32 s59, s59, s42
	v_add_u32_e32 v142, s63, v14
	v_add_u32_e32 v143, s65, v14
	s_add_i32 s63, s63, s42
	s_add_i32 s65, s65, s42
	v_lshl_add_u64 v[134:135], v[0:1], 0, s[26:27]
	s_mov_b32 s54, -2
	s_mov_b64 s[26:27], 0
	v_add_u32_e32 v141, 0, v16
	s_add_i32 s55, s19, 0xc000
	s_add_i32 s56, s19, 0xe000
	s_add_i32 s58, s57, 0x2000
	s_add_i32 s62, s59, 0x2000
	s_add_i32 s64, s63, 0x2000
	s_add_i32 s66, s65, 0x2000
	v_mov_b32_e32 v0, v131
	v_mov_b32_e32 v1, v131
	v_mov_b32_e32 v2, v131
	v_mov_b32_e32 v3, v131
	v_mov_b32_e32 v4, v131
	v_mov_b32_e32 v5, v131
	v_mov_b32_e32 v6, v131
	v_mov_b32_e32 v7, v131
	v_mov_b32_e32 v8, v131
	v_mov_b32_e32 v9, v131
	v_mov_b32_e32 v10, v131
	v_mov_b32_e32 v11, v131
	v_mov_b32_e32 v12, v131
	v_mov_b32_e32 v13, v131
	v_mov_b32_e32 v14, v131
	v_mov_b32_e32 v15, v131
	v_mov_b32_e32 v16, v131
	v_mov_b32_e32 v17, v131
	v_mov_b32_e32 v18, v131
	v_mov_b32_e32 v19, v131
	v_mov_b32_e32 v20, v131
	v_mov_b32_e32 v21, v131
	v_mov_b32_e32 v22, v131
	v_mov_b32_e32 v23, v131
	v_mov_b32_e32 v24, v131
	v_mov_b32_e32 v25, v131
	v_mov_b32_e32 v26, v131
	v_mov_b32_e32 v27, v131
	v_mov_b32_e32 v28, v131
	v_mov_b32_e32 v29, v131
	v_mov_b32_e32 v30, v131
	v_mov_b32_e32 v31, v131
	v_mov_b32_e32 v64, v131
	v_mov_b32_e32 v65, v131
	v_mov_b32_e32 v66, v131
	v_mov_b32_e32 v67, v131
	v_mov_b32_e32 v68, v131
	v_mov_b32_e32 v69, v131
	v_mov_b32_e32 v70, v131
	v_mov_b32_e32 v71, v131
	v_mov_b32_e32 v72, v131
	v_mov_b32_e32 v73, v131
	v_mov_b32_e32 v74, v131
	v_mov_b32_e32 v75, v131
	v_mov_b32_e32 v76, v131
	v_mov_b32_e32 v77, v131
	v_mov_b32_e32 v78, v131
	v_mov_b32_e32 v79, v131
	v_mov_b32_e32 v80, v131
	v_mov_b32_e32 v81, v131
	v_mov_b32_e32 v82, v131
	v_mov_b32_e32 v83, v131
	v_mov_b32_e32 v84, v131
	v_mov_b32_e32 v85, v131
	v_mov_b32_e32 v86, v131
	v_mov_b32_e32 v87, v131
	v_mov_b32_e32 v88, v131
	v_mov_b32_e32 v89, v131
	v_mov_b32_e32 v90, v131
	v_mov_b32_e32 v91, v131
	v_mov_b32_e32 v92, v131
	v_mov_b32_e32 v93, v131
	v_mov_b32_e32 v94, v131
	v_mov_b32_e32 v95, v131
	v_mov_b32_e32 v32, v131
	v_mov_b32_e32 v33, v131
	v_mov_b32_e32 v34, v131
	v_mov_b32_e32 v35, v131
	v_mov_b32_e32 v36, v131
	v_mov_b32_e32 v37, v131
	v_mov_b32_e32 v38, v131
	v_mov_b32_e32 v39, v131
	v_mov_b32_e32 v40, v131
	v_mov_b32_e32 v41, v131
	v_mov_b32_e32 v42, v131
	v_mov_b32_e32 v43, v131
	v_mov_b32_e32 v44, v131
	v_mov_b32_e32 v45, v131
	v_mov_b32_e32 v46, v131
	v_mov_b32_e32 v47, v131
	v_mov_b32_e32 v48, v131
	v_mov_b32_e32 v49, v131
	v_mov_b32_e32 v50, v131
	v_mov_b32_e32 v51, v131
	v_mov_b32_e32 v52, v131
	v_mov_b32_e32 v53, v131
	v_mov_b32_e32 v54, v131
	v_mov_b32_e32 v55, v131
	v_mov_b32_e32 v56, v131
	v_mov_b32_e32 v57, v131
	v_mov_b32_e32 v58, v131
	v_mov_b32_e32 v59, v131
	v_mov_b32_e32 v60, v131
	v_mov_b32_e32 v61, v131
	v_mov_b32_e32 v62, v131
	v_mov_b32_e32 v63, v131
	v_mov_b32_e32 v96, v131
	v_mov_b32_e32 v97, v131
	v_mov_b32_e32 v98, v131
	v_mov_b32_e32 v99, v131
	v_mov_b32_e32 v100, v131
	v_mov_b32_e32 v101, v131
	v_mov_b32_e32 v102, v131
	v_mov_b32_e32 v103, v131
	v_mov_b32_e32 v104, v131
	v_mov_b32_e32 v105, v131
	v_mov_b32_e32 v106, v131
	v_mov_b32_e32 v107, v131
	v_mov_b32_e32 v108, v131
	v_mov_b32_e32 v109, v131
	v_mov_b32_e32 v110, v131
	v_mov_b32_e32 v111, v131
	v_mov_b32_e32 v112, v131
	v_mov_b32_e32 v113, v131
	v_mov_b32_e32 v114, v131
	v_mov_b32_e32 v115, v131
	v_mov_b32_e32 v116, v131
	v_mov_b32_e32 v117, v131
	v_mov_b32_e32 v118, v131
	v_mov_b32_e32 v119, v131
	v_mov_b32_e32 v120, v131
	v_mov_b32_e32 v121, v131
	v_mov_b32_e32 v122, v131
	v_mov_b32_e32 v123, v131
	v_mov_b32_e32 v124, v131
	v_mov_b32_e32 v125, v131
	v_mov_b32_e32 v126, v131
	v_mov_b32_e32 v127, v131
	s_barrier
	.p2align 7

; #define GAS __attribute__((address_space(1)))
; __device__ __forceinline__ unsigned f2bf(float f) { unsigned u = __builtin_bit_cast(unsigned, f); return (u + 0x7fffu + ((u >> 16) & 1u)) >> 16; }
; template <int VVAR> __device__ __forceinline__ void peer_v_phase(LAS unsigned char* lds, int wave, int vcu, const unsigned char* __restrict__ VS_l, const unsigned* __restrict__ PW, bf16* __restrict__ Y) {
;     ...
; #pragma unroll 1
;     for (int it = 0; it < (VVAR == 5 ? 2 : 64); it += 2) {
;         V_HALF(pa, pb, it + 1);
;         V_HALF(pb, pa, it + 2);
;         if ((it & 3) == 2) {
;             const int blk = th * 128 + wave + 8 * (it >> 2);
;             bf16* yp = Y + ((size_t)blk * 1024 + cs * 8) * 64 + lane;
; #pragma unroll
;             for (int c = 0; c < 8; ++c) ((GAS unsigned short*)yp)[c * 64] = (unsigned short)f2bf(acc[c]);
; #pragma unroll
;             for (int c = 0; c < 8; ++c) acc[c] = 0.f;
;         }
;     }
.LBB0_935:
	s_xor_b64 s[20:21], s[20:21], -1
	s_and_b64 s[22:23], exec, s[24:25]
	s_or_b64 s[16:17], s[22:23], s[16:17]
	s_andn2_b64 s[18:19], s[18:19], exec
	s_and_b64 s[20:21], s[20:21], exec
	s_or_b64 s[18:19], s[18:19], s[20:21]
	s_andn2_b64 exec, exec, s[16:17]
	s_cbranch_execz .LBB0_942
	.p2align 7

; #define GAS __attribute__((address_space(1)))
; __device__ __forceinline__ unsigned f2bf(float f) { unsigned u = __builtin_bit_cast(unsigned, f); return (u + 0x7fffu + ((u >> 16) & 1u)) >> 16; }
; template <int VVAR> __device__ __forceinline__ void peer_v_phase(LAS unsigned char* lds, int wave, int vcu, const unsigned char* __restrict__ VS_l, const unsigned* __restrict__ PW, bf16* __restrict__ Y) {
;     ...
; #pragma unroll 1
;     for (int it = 0; it < (VVAR == 5 ? 2 : 64); it += 2) {
;         V_HALF(pa, pb, it + 1);
;         V_HALF(pb, pa, it + 2);
;         if ((it & 3) == 2) {
;             const int blk = th * 128 + wave + 8 * (it >> 2);
;             bf16* yp = Y + ((size_t)blk * 1024 + cs * 8) * 64 + lane;
; #pragma unroll
;             for (int c = 0; c < 8; ++c) ((GAS unsigned short*)yp)[c * 64] = (unsigned short)f2bf(acc[c]);
; #pragma unroll
;             for (int c = 0; c < 8; ++c) acc[c] = 0.f;
;         }
;     }
.LBB0_955:
	s_addk_i32 s16, 0x1000
	s_andn2_b64 vcc, exec, s[10:11]
	s_add_i32 s3, s3, 4
	s_cbranch_vccz .LBB0_958
	.p2align 7

; #define PG8_STAGE(bufoff, gbase, voff) do { _Pragma("unroll") for (int _i = 0; _i < 2; ++_i) \
;         __builtin_amdgcn_global_load_lds((const unsigned*)((const char*)(gbase) + (voff)[_i]), (PG8_LAS unsigned*)(lds + (bufoff) + ldsw + _i * 8192), 16, 0, 0); } while (0)
; #define PG8_WAIT_V(n) asm volatile("s_waitcnt vmcnt(" #n ")" ::: "memory")
; #define PG8_BAR __builtin_amdgcn_s_barrier()
; template <class Epi, class Sched, bool ALIGN_EPI = false, bool SP2 = false>
; __device__ __forceinline__ void gemm_phase(int wave_id  , PG8_LAS unsigned char* lds, const Gemm g, const Sched& S, const Epi& E) {
;     ...
;     f32x4 acc[2][2][4][2];
; #pragma unroll
;     for (int a = 0; a < 2; ++a)
; #pragma unroll
;         for (int b = 0; b < 2; ++b)
; #pragma unroll
;             for (int m = 0; m < 4; ++m)
; #pragma unroll
;                 for (int n = 0; n < 2; ++n) acc[a][b][m][n] = (f32x4){0.f, 0.f, 0.f, 0.f};
;     bf16x8 At[4][2], B0[2][2], B1[2][2];
;     const char* cA = (const char*)g.A + (size_t)cur.pm * tstep; const char* cB = (const char*)g.Bt + (size_t)cur.pn * tstep;
;     S.a_ready(cur);
;     if constexpr (SP2) {
;         PG8_STAGE(PG8_SB(0, 0), cB, voffB); PG8_STAGE(PG8_SB(0, 1), cB + hstep, voffB); PG8_STAGE(PG8_SA(0, 0), cA, voffA); PG8_STAGE(PG8_SA(0, 1), cA + hstep, voffA);
;         if (wr == 1) PG8_BAR;
;         PG8_WAIT_V(2); PG8_BAR;
;         PG8_STAGE(PG8_SB(1, 0), cB + kstep, voffB); PG8_STAGE(PG8_SA(1, 0), cA + kstep, voffA); PG8_STAGE(PG8_SB(1, 1), cB + hstep + kstep, voffB);
;         PG8_WAIT_V(6); PG8_BAR;
.LBB0_1433:
	v_and_b32_e32 v145, 15, v144
	v_and_b32_e32 v14, 48, v144
	v_lshlrev_b32_e32 v15, 2, v144
	s_mov_b64 s[20:21], 0x80
	s_sext_i32_i8 s8, s4
	s_and_b32 s17, s48, 3
	s_lshl_b32 s4, s9, 13
	v_lshl_or_b32 v14, v145, 6, v14
	v_and_b32_e32 v15, 32, v15
	s_add_i32 m0, s56, 0x18000
	v_lshl_add_u64 v[6:7], v[6:7], 0, s[20:21]
	s_lshl_b32 s57, s9, 6
	v_bitop3_b32 v16, v14, s4, v15 bitop3:0xde
	s_lshl_b32 s4, s17, 12
	s_waitcnt vmcnt(2)
	s_barrier
	global_load_lds_dwordx4 v[6:7], off
	v_lshl_add_u64 v[4:5], v[4:5], 0, s[20:21]
	s_add_i32 m0, s56, 0x1a000
	s_add_i32 s65, s56, 0x8000
	s_add_i32 s66, s56, 0xa000
	global_load_lds_dwordx4 v[4:5], off
	v_lshl_add_u64 v[2:3], v[2:3], 0, s[20:21]
	s_mov_b32 m0, s65
	s_add_u32 s6, s42, 0x40080
	global_load_lds_dwordx4 v[2:3], off
	v_lshl_add_u64 v[0:1], v[0:1], 0, s[20:21]
	s_mov_b32 m0, s66
	s_addc_u32 s7, s43, 0
	global_load_lds_dwordx4 v[0:1], off
	s_add_i32 m0, s56, 0x1c000
	v_lshl_add_u64 v[0:1], s[6:7], 0, v[128:129]
	global_load_lds_dwordx4 v[0:1], off
	v_lshl_add_u64 v[0:1], s[6:7], 0, v[130:131]
	s_add_i32 m0, s56, 0x1e000
	v_bitop3_b32 v146, v14, s4, v15 bitop3:0xde
	global_load_lds_dwordx4 v[0:1], off
	v_lshlrev_b32_e32 v0, 14, v8
	v_and_b32_e32 v0, 0xffff8000, v0
	v_lshl_add_u32 v0, v9, 11, v0
	v_and_b32_e32 v1, 1, v8
	v_lshl_or_b32 v0, v1, 6, v0
	s_mov_b64 s[4:5], 0x40080
	v_lshl_add_u32 v0, v10, 1, v0
	v_mov_b32_e32 v1, 0
	v_lshl_add_u64 v[132:133], v[0:1], 0, s[4:5]
	v_lshlrev_b32_e32 v0, 14, v11
	v_and_b32_e32 v0, 0xffff8000, v0
	v_lshl_add_u32 v0, v12, 11, v0
	v_and_b32_e32 v2, 1, v11
	s_waitcnt vmcnt(6)
	v_lshl_or_b32 v0, v2, 6, v0
	v_lshl_add_u32 v0, v13, 1, v0
	v_or_b32_e32 v160, s57, v145
	s_mov_b32 s64, 0
	v_lshl_add_u64 v[134:135], v[0:1], 0, s[4:5]
	v_mov_b64_e32 v[136:137], 0x100
	v_mov_b64_e32 v[138:139], 0xff
	s_add_i32 s67, 0, 0x10000
	s_add_i32 s68, 0, 0x14000
	v_add_u32_e32 v147, 0, v16
	v_mov_b32_e32 v0, v1
	v_mov_b32_e32 v2, v1
	v_mov_b32_e32 v3, v1
	v_mov_b32_e32 v4, v1
	v_mov_b32_e32 v5, v1
	v_mov_b32_e32 v6, v1
	v_mov_b32_e32 v7, v1
	v_mov_b32_e32 v16, v1
	v_mov_b32_e32 v17, v1
	v_mov_b32_e32 v18, v1
	v_mov_b32_e32 v19, v1
	v_mov_b32_e32 v20, v1
	v_mov_b32_e32 v21, v1
	v_mov_b32_e32 v22, v1
	v_mov_b32_e32 v23, v1
	v_mov_b32_e32 v32, v1
	v_mov_b32_e32 v33, v1
	v_mov_b32_e32 v34, v1
	v_mov_b32_e32 v35, v1
	v_mov_b32_e32 v40, v1
	v_mov_b32_e32 v41, v1
	v_mov_b32_e32 v42, v1
	v_mov_b32_e32 v43, v1
	v_mov_b32_e32 v36, v1
	v_mov_b32_e32 v37, v1
	v_mov_b32_e32 v38, v1
	v_mov_b32_e32 v39, v1
	v_mov_b32_e32 v44, v1
	v_mov_b32_e32 v45, v1
	v_mov_b32_e32 v46, v1
	v_mov_b32_e32 v47, v1
	v_mov_b32_e32 v8, v1
	v_mov_b32_e32 v9, v1
	v_mov_b32_e32 v10, v1
	v_mov_b32_e32 v11, v1
	v_mov_b32_e32 v12, v1
	v_mov_b32_e32 v13, v1
	v_mov_b32_e32 v14, v1
	v_mov_b32_e32 v15, v1
	v_mov_b32_e32 v24, v1
	v_mov_b32_e32 v25, v1
	v_mov_b32_e32 v26, v1
	v_mov_b32_e32 v27, v1
	v_mov_b32_e32 v28, v1
	v_mov_b32_e32 v29, v1
	v_mov_b32_e32 v30, v1
	v_mov_b32_e32 v31, v1
	v_mov_b32_e32 v48, v1
	v_mov_b32_e32 v49, v1
	v_mov_b32_e32 v50, v1
	v_mov_b32_e32 v51, v1
	v_mov_b32_e32 v56, v1
	v_mov_b32_e32 v57, v1
	v_mov_b32_e32 v58, v1
	v_mov_b32_e32 v59, v1
	v_mov_b32_e32 v52, v1
	v_mov_b32_e32 v53, v1
	v_mov_b32_e32 v54, v1
	v_mov_b32_e32 v55, v1
	v_mov_b32_e32 v60, v1
	v_mov_b32_e32 v61, v1
	v_mov_b32_e32 v62, v1
	v_mov_b32_e32 v63, v1
	v_mov_b32_e32 v64, v1
	v_mov_b32_e32 v65, v1
	v_mov_b32_e32 v66, v1
	v_mov_b32_e32 v67, v1
	v_mov_b32_e32 v72, v1
	v_mov_b32_e32 v73, v1
	v_mov_b32_e32 v74, v1
	v_mov_b32_e32 v75, v1
	v_mov_b32_e32 v68, v1
	v_mov_b32_e32 v69, v1
	v_mov_b32_e32 v70, v1
	v_mov_b32_e32 v71, v1
	v_mov_b32_e32 v80, v1
	v_mov_b32_e32 v81, v1
	v_mov_b32_e32 v82, v1
	v_mov_b32_e32 v83, v1
	v_mov_b32_e32 v76, v1
	v_mov_b32_e32 v77, v1
	v_mov_b32_e32 v78, v1
	v_mov_b32_e32 v79, v1
	v_mov_b32_e32 v88, v1
	v_mov_b32_e32 v89, v1
	v_mov_b32_e32 v90, v1
	v_mov_b32_e32 v91, v1
	v_mov_b32_e32 v100, v1
	v_mov_b32_e32 v101, v1
	v_mov_b32_e32 v102, v1
	v_mov_b32_e32 v103, v1
	v_mov_b32_e32 v112, v1
	v_mov_b32_e32 v113, v1
	v_mov_b32_e32 v114, v1
	v_mov_b32_e32 v115, v1
	v_mov_b32_e32 v84, v1
	v_mov_b32_e32 v85, v1
	v_mov_b32_e32 v86, v1
	v_mov_b32_e32 v87, v1
	v_mov_b32_e32 v96, v1
	v_mov_b32_e32 v97, v1
	v_mov_b32_e32 v98, v1
	v_mov_b32_e32 v99, v1
	v_mov_b32_e32 v92, v1
	v_mov_b32_e32 v93, v1
	v_mov_b32_e32 v94, v1
	v_mov_b32_e32 v95, v1
	v_mov_b32_e32 v108, v1
	v_mov_b32_e32 v109, v1
	v_mov_b32_e32 v110, v1
	v_mov_b32_e32 v111, v1
	v_mov_b32_e32 v104, v1
	v_mov_b32_e32 v105, v1
	v_mov_b32_e32 v106, v1
	v_mov_b32_e32 v107, v1
	v_mov_b32_e32 v116, v1
	v_mov_b32_e32 v117, v1
	v_mov_b32_e32 v118, v1
	v_mov_b32_e32 v119, v1
	v_mov_b32_e32 v120, v1
	v_mov_b32_e32 v121, v1
	v_mov_b32_e32 v122, v1
	v_mov_b32_e32 v123, v1
	v_mov_b32_e32 v124, v1
	v_mov_b32_e32 v125, v1
	v_mov_b32_e32 v126, v1
	v_mov_b32_e32 v127, v1
	s_barrier
	.p2align 7

; #define PG8_STAGE(bufoff, gbase, voff) do { _Pragma("unroll") for (int _i = 0; _i < 2; ++_i) \
;         __builtin_amdgcn_global_load_lds((const unsigned*)((const char*)(gbase) + (voff)[_i]), (PG8_LAS unsigned*)(lds + (bufoff) + ldsw + _i * 8192), 16, 0, 0); } while (0)
; #define PG8_WAIT_V(n) asm volatile("s_waitcnt vmcnt(" #n ")" ::: "memory")
; #define PG8_BAR __builtin_amdgcn_s_barrier()
; template <class Epi, class Sched, bool ALIGN_EPI = false, bool SP2 = false>
; __device__ __forceinline__ void gemm_phase(int wave_id  , PG8_LAS unsigned char* lds, const Gemm g, const Sched& S, const Epi& E) {
;     ...
;     f32x4 acc[2][2][4][2];
; #pragma unroll
;     for (int a = 0; a < 2; ++a)
; #pragma unroll
;         for (int b = 0; b < 2; ++b)
; #pragma unroll
;             for (int m = 0; m < 4; ++m)
; #pragma unroll
;                 for (int n = 0; n < 2; ++n) acc[a][b][m][n] = (f32x4){0.f, 0.f, 0.f, 0.f};
;     bf16x8 At[4][2], B0[2][2], B1[2][2];
;     const char* cA = (const char*)g.A + (size_t)cur.pm * tstep; const char* cB = (const char*)g.Bt + (size_t)cur.pn * tstep;
;     S.a_ready(cur);
;     if constexpr (SP2) {
;         PG8_STAGE(PG8_SB(0, 0), cB, voffB); PG8_STAGE(PG8_SB(0, 1), cB + hstep, voffB); PG8_STAGE(PG8_SA(0, 0), cA, voffA); PG8_STAGE(PG8_SA(0, 1), cA + hstep, voffA);
;         if (wr == 1) PG8_BAR;
;         PG8_WAIT_V(2); PG8_BAR;
;         PG8_STAGE(PG8_SB(1, 0), cB + kstep, voffB); PG8_STAGE(PG8_SA(1, 0), cA + kstep, voffA); PG8_STAGE(PG8_SB(1, 1), cB + hstep + kstep, voffB);
;         PG8_WAIT_V(6); PG8_BAR;
.LBB0_1572:
	v_and_b32_e32 v138, 15, v139
	v_and_b32_e32 v14, 48, v139
	v_lshlrev_b32_e32 v15, 2, v139
	s_and_b32 s57, s51, 3
	v_lshl_or_b32 v14, v138, 6, v14
	s_lshl_b32 s24, s52, 13
	v_and_b32_e32 v15, 32, v15
	v_bitop3_b32 v16, v14, s24, v15 bitop3:0xde
	s_lshl_b32 s24, s57, 12
	v_bitop3_b32 v14, v14, s24, v15 bitop3:0xde
	s_mov_b64 s[24:25], 0x80
	s_add_i32 m0, s19, 0x18000
	v_lshl_add_u64 v[6:7], v[6:7], 0, s[24:25]
	s_waitcnt vmcnt(2)
	s_barrier
	global_load_lds_dwordx4 v[6:7], off
	v_lshl_add_u64 v[4:5], v[4:5], 0, s[24:25]
	s_add_i32 m0, s19, 0x1a000
	s_add_i32 s58, s19, 0x8000
	s_add_i32 s59, s19, 0xa000
	global_load_lds_dwordx4 v[4:5], off
	v_lshl_add_u64 v[0:1], v[0:1], 0, s[24:25]
	s_mov_b32 m0, s58
	s_add_u32 s34, s4, 0x40080
	global_load_lds_dwordx4 v[0:1], off
	v_lshl_add_u64 v[0:1], v[2:3], 0, s[24:25]
	s_mov_b32 m0, s59
	s_addc_u32 s35, s5, 0
	global_load_lds_dwordx4 v[0:1], off
	s_add_i32 m0, s19, 0x1c000
	v_lshl_add_u64 v[0:1], s[34:35], 0, v[130:131]
	global_load_lds_dwordx4 v[0:1], off
	v_lshl_add_u64 v[0:1], s[34:35], 0, v[128:129]
	s_add_i32 m0, s19, 0x1e000
	s_add_u32 s26, s14, s26
	global_load_lds_dwordx4 v[0:1], off
	s_addc_u32 s27, s15, s27
	s_add_u32 s62, s26, 0x1400100
	s_addc_u32 s63, s27, 0
	s_sub_i32 s26, s28, s44
	s_lshl_b32 s27, s43, 5
	s_sub_i32 s26, s26, s27
	s_sext_i32_i8 s26, s26
	s_add_i32 s26, s29, s26
	v_lshlrev_b32_e32 v0, 14, v8
	s_ashr_i32 s27, s26, 31
	v_and_b32_e32 v0, 0xffff8000, v0
	s_lshl_b64 s[26:27], s[26:27], 19
	v_lshl_add_u32 v0, v10, 11, v0
	v_and_b32_e32 v1, 1, v8
	v_lshl_or_b32 v0, v1, 6, v0
	s_add_u32 s26, s14, s26
	v_lshl_add_u32 v0, v11, 1, v0
	v_mov_b32_e32 v1, v131
	s_addc_u32 s27, s15, s27
	v_lshl_add_u64 v[0:1], s[26:27], 0, v[0:1]
	s_mov_b64 s[28:29], 0x6040080
	v_lshl_add_u64 v[132:133], v[0:1], 0, s[28:29]
	v_lshlrev_b32_e32 v0, 14, v9
	v_and_b32_e32 v0, 0xffff8000, v0
	v_lshl_add_u32 v0, v12, 11, v0
	v_and_b32_e32 v1, 1, v9
	v_lshl_or_b32 v0, v1, 6, v0
	s_waitcnt vmcnt(6)
	v_lshl_add_u32 v0, v13, 1, v0
	v_mov_b32_e32 v1, v131
	s_add_i32 s67, 0, 0x10000
	s_add_i32 s69, 0, 0x14000
	s_add_i32 s71, 0, 0x18000
	s_add_i32 s73, 0, 0x1c000
	v_lshl_add_u64 v[0:1], s[26:27], 0, v[0:1]
	v_add_u32_e32 v140, s67, v14
	v_add_u32_e32 v141, s69, v14
	s_add_i32 s67, s67, s42
	s_add_i32 s69, s69, s42
	v_add_u32_e32 v143, s71, v14
	v_add_u32_e32 v144, s73, v14
	s_add_i32 s71, s71, s42
	s_add_i32 s73, s73, s42
	v_lshl_add_u64 v[134:135], v[0:1], 0, s[28:29]
	s_mov_b32 s64, -2
	s_mov_b64 s[28:29], 0
	v_add_u32_e32 v142, 0, v16
	s_add_i32 s65, s19, 0xc000
	s_add_i32 s66, s19, 0xe000
	s_add_i32 s68, s67, 0x2000
	s_add_i32 s70, s69, 0x2000
	s_add_i32 s72, s71, 0x2000
	s_add_i32 s74, s73, 0x2000
	v_mov_b32_e32 v0, v131
	v_mov_b32_e32 v1, v131
	v_mov_b32_e32 v2, v131
	v_mov_b32_e32 v3, v131
	v_mov_b32_e32 v4, v131
	v_mov_b32_e32 v5, v131
	v_mov_b32_e32 v6, v131
	v_mov_b32_e32 v7, v131
	v_mov_b32_e32 v8, v131
	v_mov_b32_e32 v9, v131
	v_mov_b32_e32 v10, v131
	v_mov_b32_e32 v11, v131
	v_mov_b32_e32 v12, v131
	v_mov_b32_e32 v13, v131
	v_mov_b32_e32 v14, v131
	v_mov_b32_e32 v15, v131
	v_mov_b32_e32 v16, v131
	v_mov_b32_e32 v17, v131
	v_mov_b32_e32 v18, v131
	v_mov_b32_e32 v19, v131
	v_mov_b32_e32 v20, v131
	v_mov_b32_e32 v21, v131
	v_mov_b32_e32 v22, v131
	v_mov_b32_e32 v23, v131
	v_mov_b32_e32 v24, v131
	v_mov_b32_e32 v25, v131
	v_mov_b32_e32 v26, v131
	v_mov_b32_e32 v27, v131
	v_mov_b32_e32 v28, v131
	v_mov_b32_e32 v29, v131
	v_mov_b32_e32 v30, v131
	v_mov_b32_e32 v31, v131
	v_mov_b32_e32 v64, v131
	v_mov_b32_e32 v65, v131
	v_mov_b32_e32 v66, v131
	v_mov_b32_e32 v67, v131
	v_mov_b32_e32 v68, v131
	v_mov_b32_e32 v69, v131
	v_mov_b32_e32 v70, v131
	v_mov_b32_e32 v71, v131
	v_mov_b32_e32 v72, v131
	v_mov_b32_e32 v73, v131
	v_mov_b32_e32 v74, v131
	v_mov_b32_e32 v75, v131
	v_mov_b32_e32 v76, v131
	v_mov_b32_e32 v77, v131
	v_mov_b32_e32 v78, v131
	v_mov_b32_e32 v79, v131
	v_mov_b32_e32 v80, v131
	v_mov_b32_e32 v81, v131
	v_mov_b32_e32 v82, v131
	v_mov_b32_e32 v83, v131
	v_mov_b32_e32 v84, v131
	v_mov_b32_e32 v85, v131
	v_mov_b32_e32 v86, v131
	v_mov_b32_e32 v87, v131
	v_mov_b32_e32 v88, v131
	v_mov_b32_e32 v89, v131
	v_mov_b32_e32 v90, v131
	v_mov_b32_e32 v91, v131
	v_mov_b32_e32 v92, v131
	v_mov_b32_e32 v93, v131
	v_mov_b32_e32 v94, v131
	v_mov_b32_e32 v95, v131
	v_mov_b32_e32 v32, v131
	v_mov_b32_e32 v33, v131
	v_mov_b32_e32 v34, v131
	v_mov_b32_e32 v35, v131
	v_mov_b32_e32 v36, v131
	v_mov_b32_e32 v37, v131
	v_mov_b32_e32 v38, v131
	v_mov_b32_e32 v39, v131
	v_mov_b32_e32 v40, v131
	v_mov_b32_e32 v41, v131
	v_mov_b32_e32 v42, v131
	v_mov_b32_e32 v43, v131
	v_mov_b32_e32 v44, v131
	v_mov_b32_e32 v45, v131
	v_mov_b32_e32 v46, v131
	v_mov_b32_e32 v47, v131
	v_mov_b32_e32 v48, v131
	v_mov_b32_e32 v49, v131
	v_mov_b32_e32 v50, v131
	v_mov_b32_e32 v51, v131
	v_mov_b32_e32 v52, v131
	v_mov_b32_e32 v53, v131
	v_mov_b32_e32 v54, v131
	v_mov_b32_e32 v55, v131
	v_mov_b32_e32 v56, v131
	v_mov_b32_e32 v57, v131
	v_mov_b32_e32 v58, v131
	v_mov_b32_e32 v59, v131
	v_mov_b32_e32 v60, v131
	v_mov_b32_e32 v61, v131
	v_mov_b32_e32 v62, v131
	v_mov_b32_e32 v63, v131
	v_mov_b32_e32 v96, v131
	v_mov_b32_e32 v97, v131
	v_mov_b32_e32 v98, v131
	v_mov_b32_e32 v99, v131
	v_mov_b32_e32 v100, v131
	v_mov_b32_e32 v101, v131
	v_mov_b32_e32 v102, v131
	v_mov_b32_e32 v103, v131
	v_mov_b32_e32 v104, v131
	v_mov_b32_e32 v105, v131
	v_mov_b32_e32 v106, v131
	v_mov_b32_e32 v107, v131
	v_mov_b32_e32 v108, v131
	v_mov_b32_e32 v109, v131
	v_mov_b32_e32 v110, v131
	v_mov_b32_e32 v111, v131
	v_mov_b32_e32 v112, v131
	v_mov_b32_e32 v113, v131
	v_mov_b32_e32 v114, v131
	v_mov_b32_e32 v115, v131
	v_mov_b32_e32 v116, v131
	v_mov_b32_e32 v117, v131
	v_mov_b32_e32 v118, v131
	v_mov_b32_e32 v119, v131
	v_mov_b32_e32 v120, v131
	v_mov_b32_e32 v121, v131
	v_mov_b32_e32 v122, v131
	v_mov_b32_e32 v123, v131
	v_mov_b32_e32 v124, v131
	v_mov_b32_e32 v125, v131
	v_mov_b32_e32 v126, v131
	v_mov_b32_e32 v127, v131
	s_barrier
	.p2align 7

; #define PG8_STAGE(bufoff, gbase, voff) do { _Pragma("unroll") for (int _i = 0; _i < 2; ++_i) \
;         __builtin_amdgcn_global_load_lds((const unsigned*)((const char*)(gbase) + (voff)[_i]), (PG8_LAS unsigned*)(lds + (bufoff) + ldsw + _i * 8192), 16, 0, 0); } while (0)
; #define PG8_WAIT_V(n) asm volatile("s_waitcnt vmcnt(" #n ")" ::: "memory")
; #define PG8_BAR __builtin_amdgcn_s_barrier()
; template <class Epi, class Sched, bool ALIGN_EPI = false, bool SP2 = false>
; __device__ __forceinline__ void gemm_phase(int wave_id  , PG8_LAS unsigned char* lds, const Gemm g, const Sched& S, const Epi& E) {
;     ...
;     f32x4 acc[2][2][4][2];
; #pragma unroll
;     for (int a = 0; a < 2; ++a)
; #pragma unroll
;         for (int b = 0; b < 2; ++b)
; #pragma unroll
;             for (int m = 0; m < 4; ++m)
; #pragma unroll
;                 for (int n = 0; n < 2; ++n) acc[a][b][m][n] = (f32x4){0.f, 0.f, 0.f, 0.f};
;     bf16x8 At[4][2], B0[2][2], B1[2][2];
;     const char* cA = (const char*)g.A + (size_t)cur.pm * tstep; const char* cB = (const char*)g.Bt + (size_t)cur.pn * tstep;
;     S.a_ready(cur);
;     if constexpr (SP2) {
;         PG8_STAGE(PG8_SB(0, 0), cB, voffB); PG8_STAGE(PG8_SB(0, 1), cB + hstep, voffB); PG8_STAGE(PG8_SA(0, 0), cA, voffA); PG8_STAGE(PG8_SA(0, 1), cA + hstep, voffA);
;         if (wr == 1) PG8_BAR;
;         PG8_WAIT_V(2); PG8_BAR;
;         PG8_STAGE(PG8_SB(1, 0), cB + kstep, voffB); PG8_STAGE(PG8_SA(1, 0), cA + kstep, voffA); PG8_STAGE(PG8_SB(1, 1), cB + hstep + kstep, voffB);
;         PG8_WAIT_V(6); PG8_BAR;
.LBB0_1590:
	v_and_b32_e32 v138, 15, v137
	v_and_b32_e32 v14, 48, v137
	v_lshlrev_b32_e32 v15, 2, v137
	s_and_b32 s48, s44, 3
	v_lshl_or_b32 v14, v138, 6, v14
	s_lshl_b32 s24, s45, 13
	v_and_b32_e32 v15, 32, v15
	v_bitop3_b32 v16, v14, s24, v15 bitop3:0xde
	s_lshl_b32 s24, s48, 12
	v_bitop3_b32 v14, v14, s24, v15 bitop3:0xde
	s_mov_b64 s[24:25], 0x80
	s_add_i32 m0, s19, 0x18000
	v_lshl_add_u64 v[6:7], v[6:7], 0, s[24:25]
	s_waitcnt vmcnt(2)
	s_barrier
	global_load_lds_dwordx4 v[6:7], off
	v_lshl_add_u64 v[4:5], v[4:5], 0, s[24:25]
	s_add_i32 m0, s19, 0x1a000
	s_add_i32 s50, s19, 0x8000
	s_add_i32 s51, s19, 0xa000
	global_load_lds_dwordx4 v[4:5], off
	v_lshl_add_u64 v[0:1], v[0:1], 0, s[24:25]
	s_mov_b32 m0, s50
	s_add_u32 s34, s4, 0x40080
	global_load_lds_dwordx4 v[0:1], off
	v_lshl_add_u64 v[0:1], v[2:3], 0, s[24:25]
	s_mov_b32 m0, s51
	s_addc_u32 s35, s5, 0
	global_load_lds_dwordx4 v[0:1], off
	s_add_i32 m0, s19, 0x1c000
	v_lshl_add_u64 v[0:1], s[34:35], 0, v[130:131]
	global_load_lds_dwordx4 v[0:1], off
	v_lshl_add_u64 v[0:1], s[34:35], 0, v[128:129]
	s_add_i32 m0, s19, 0x1e000
	s_add_u32 s28, s14, s28
	global_load_lds_dwordx4 v[0:1], off
	s_addc_u32 s29, s15, s29
	v_lshlrev_b32_e32 v0, 14, v8
	s_add_u32 s52, s28, 0x1400100
	v_and_b32_e32 v0, 0xffff8000, v0
	s_addc_u32 s53, s29, 0
	v_lshl_add_u32 v0, v10, 11, v0
	v_and_b32_e32 v1, 1, v8
	v_lshl_or_b32 v0, v1, 6, v0
	s_add_u32 s14, s14, s26
	v_lshl_add_u32 v0, v11, 1, v0
	v_mov_b32_e32 v1, v131
	s_addc_u32 s15, s15, s27
	v_lshl_add_u64 v[0:1], s[14:15], 0, v[0:1]
	s_mov_b64 s[26:27], 0x6040080
	v_lshl_add_u64 v[132:133], v[0:1], 0, s[26:27]
	v_lshlrev_b32_e32 v0, 14, v9
	v_and_b32_e32 v0, 0xffff8000, v0
	v_lshl_add_u32 v0, v12, 11, v0
	v_and_b32_e32 v1, 1, v9
	v_lshl_or_b32 v0, v1, 6, v0
	s_waitcnt vmcnt(6)
	v_lshl_add_u32 v0, v13, 1, v0
	v_mov_b32_e32 v1, v131
	s_add_i32 s57, 0, 0x10000
	s_add_i32 s59, 0, 0x14000
	s_add_i32 s63, 0, 0x18000
	s_add_i32 s65, 0, 0x1c000
	v_lshl_add_u64 v[0:1], s[14:15], 0, v[0:1]
	v_add_u32_e32 v139, s57, v14
	v_add_u32_e32 v140, s59, v14
	s_add_i32 s57, s57, s42
	s_add_i32 s59, s59, s42
	v_add_u32_e32 v142, s63, v14
	v_add_u32_e32 v143, s65, v14
	s_add_i32 s63, s63, s42
	s_add_i32 s65, s65, s42
	v_lshl_add_u64 v[134:135], v[0:1], 0, s[26:27]
	s_mov_b32 s54, -2
	s_mov_b64 s[26:27], 0
	v_add_u32_e32 v141, 0, v16
	s_add_i32 s55, s19, 0xc000
	s_add_i32 s56, s19, 0xe000
	s_add_i32 s58, s57, 0x2000
	s_add_i32 s62, s59, 0x2000
	s_add_i32 s64, s63, 0x2000
	s_add_i32 s66, s65, 0x2000
	v_mov_b32_e32 v0, v131
	v_mov_b32_e32 v1, v131
	v_mov_b32_e32 v2, v131
	v_mov_b32_e32 v3, v131
	v_mov_b32_e32 v4, v131
	v_mov_b32_e32 v5, v131
	v_mov_b32_e32 v6, v131
	v_mov_b32_e32 v7, v131
	v_mov_b32_e32 v8, v131
	v_mov_b32_e32 v9, v131
	v_mov_b32_e32 v10, v131
	v_mov_b32_e32 v11, v131
	v_mov_b32_e32 v12, v131
	v_mov_b32_e32 v13, v131
	v_mov_b32_e32 v14, v131
	v_mov_b32_e32 v15, v131
	v_mov_b32_e32 v16, v131
	v_mov_b32_e32 v17, v131
	v_mov_b32_e32 v18, v131
	v_mov_b32_e32 v19, v131
	v_mov_b32_e32 v20, v131
	v_mov_b32_e32 v21, v131
	v_mov_b32_e32 v22, v131
	v_mov_b32_e32 v23, v131
	v_mov_b32_e32 v24, v131
	v_mov_b32_e32 v25, v131
	v_mov_b32_e32 v26, v131
	v_mov_b32_e32 v27, v131
	v_mov_b32_e32 v28, v131
	v_mov_b32_e32 v29, v131
	v_mov_b32_e32 v30, v131
	v_mov_b32_e32 v31, v131
	v_mov_b32_e32 v64, v131
	v_mov_b32_e32 v65, v131
	v_mov_b32_e32 v66, v131
	v_mov_b32_e32 v67, v131
	v_mov_b32_e32 v68, v131
	v_mov_b32_e32 v69, v131
	v_mov_b32_e32 v70, v131
	v_mov_b32_e32 v71, v131
	v_mov_b32_e32 v72, v131
	v_mov_b32_e32 v73, v131
	v_mov_b32_e32 v74, v131
	v_mov_b32_e32 v75, v131
	v_mov_b32_e32 v76, v131
	v_mov_b32_e32 v77, v131
	v_mov_b32_e32 v78, v131
	v_mov_b32_e32 v79, v131
	v_mov_b32_e32 v80, v131
	v_mov_b32_e32 v81, v131
	v_mov_b32_e32 v82, v131
	v_mov_b32_e32 v83, v131
	v_mov_b32_e32 v84, v131
	v_mov_b32_e32 v85, v131
	v_mov_b32_e32 v86, v131
	v_mov_b32_e32 v87, v131
	v_mov_b32_e32 v88, v131
	v_mov_b32_e32 v89, v131
	v_mov_b32_e32 v90, v131
	v_mov_b32_e32 v91, v131
	v_mov_b32_e32 v92, v131
	v_mov_b32_e32 v93, v131
	v_mov_b32_e32 v94, v131
	v_mov_b32_e32 v95, v131
	v_mov_b32_e32 v32, v131
	v_mov_b32_e32 v33, v131
	v_mov_b32_e32 v34, v131
	v_mov_b32_e32 v35, v131
	v_mov_b32_e32 v36, v131
	v_mov_b32_e32 v37, v131
	v_mov_b32_e32 v38, v131
	v_mov_b32_e32 v39, v131
	v_mov_b32_e32 v40, v131
	v_mov_b32_e32 v41, v131
	v_mov_b32_e32 v42, v131
	v_mov_b32_e32 v43, v131
	v_mov_b32_e32 v44, v131
	v_mov_b32_e32 v45, v131
	v_mov_b32_e32 v46, v131
	v_mov_b32_e32 v47, v131
	v_mov_b32_e32 v48, v131
	v_mov_b32_e32 v49, v131
	v_mov_b32_e32 v50, v131
	v_mov_b32_e32 v51, v131
	v_mov_b32_e32 v52, v131
	v_mov_b32_e32 v53, v131
	v_mov_b32_e32 v54, v131
	v_mov_b32_e32 v55, v131
	v_mov_b32_e32 v56, v131
	v_mov_b32_e32 v57, v131
	v_mov_b32_e32 v58, v131
	v_mov_b32_e32 v59, v131
	v_mov_b32_e32 v60, v131
	v_mov_b32_e32 v61, v131
	v_mov_b32_e32 v62, v131
	v_mov_b32_e32 v63, v131
	v_mov_b32_e32 v96, v131
	v_mov_b32_e32 v97, v131
	v_mov_b32_e32 v98, v131
	v_mov_b32_e32 v99, v131
	v_mov_b32_e32 v100, v131
	v_mov_b32_e32 v101, v131
	v_mov_b32_e32 v102, v131
	v_mov_b32_e32 v103, v131
	v_mov_b32_e32 v104, v131
	v_mov_b32_e32 v105, v131
	v_mov_b32_e32 v106, v131
	v_mov_b32_e32 v107, v131
	v_mov_b32_e32 v108, v131
	v_mov_b32_e32 v109, v131
	v_mov_b32_e32 v110, v131
	v_mov_b32_e32 v111, v131
	v_mov_b32_e32 v112, v131
	v_mov_b32_e32 v113, v131
	v_mov_b32_e32 v114, v131
	v_mov_b32_e32 v115, v131
	v_mov_b32_e32 v116, v131
	v_mov_b32_e32 v117, v131
	v_mov_b32_e32 v118, v131
	v_mov_b32_e32 v119, v131
	v_mov_b32_e32 v120, v131
	v_mov_b32_e32 v121, v131
	v_mov_b32_e32 v122, v131
	v_mov_b32_e32 v123, v131
	v_mov_b32_e32 v124, v131
	v_mov_b32_e32 v125, v131
	v_mov_b32_e32 v126, v131
	v_mov_b32_e32 v127, v131
	s_barrier
	.p2align 7
